# stagger the in-FFN1 weight conversion: workgroups with id bit 3 set convert on odd units, the others on even units (halves the HBM burst per epilogue)
# baseline (speedup 1.0000x reference)
.LBB0_1912:
	s_lshr_b32 s72, s2, 3
	s_xor_b32 s72, s72, s32
	s_and_b32 s72, s72, 1
	s_cbranch_scc1 .Lcvd_p1_end
	s_cmpk_ge_u32 s32, 14
	s_cbranch_scc1 .Lcvd_p1_end
	v_readlane_b32 s72, v255, 44
	s_lshr_b32 s80, s32, 1
	s_lshl_b32 s80, s80, 10
	s_add_i32 s80, s80, s2
	s_nop 0
	s_add_i32 s72, s72, s80
	s_cmpk_ge_i32 s72, 7136
	s_cbranch_scc1 .Lcvd_p1_end
	s_addk_i32 s72, 1056
	v_readlane_b32 s78, v255, 40
	v_readlane_b32 s79, v255, 41
	s_lshr_b32 s80, s72, 4
	s_lshl_b32 s80, s80, 18
	s_and_b32 s81, s72, 15
	s_lshl_b32 s81, s81, 8
	s_add_i32 s80, s80, s81
	v_bfe_u32 v24, v0, 4, 2
	v_lshlrev_b32_e32 v24, 15, v24
	v_and_b32_e32 v210, 15, v0
	v_lshl_add_u32 v24, v210, 4, v24
	v_add_u32_e32 v24, s80, v24
	v_add_u32_e32 v214, 0x1000, v24
	v_add_u32_e32 v218, 0x2000, v24
	v_add_u32_e32 v222, 0x3000, v24
	v_add_u32_e32 v230, 0x4000, v24
	v_add_u32_e32 v234, 0x5000, v24
	v_add_u32_e32 v240, 0x6000, v24
	v_add_u32_e32 v244, 0x7000, v24
	global_load_dwordx4 v[210:213], v24, s[78:79]
	global_load_dwordx4 v[214:217], v214, s[78:79]
	global_load_dwordx4 v[218:221], v218, s[78:79]
	global_load_dwordx4 v[222:225], v222, s[78:79]
	global_load_dwordx4 v[230:233], v230, s[78:79]
	global_load_dwordx4 v[234:237], v234, s[78:79]
	global_load_dwordx4 v[240:243], v240, s[78:79]
	global_load_dwordx4 v[244:247], v244, s[78:79]
.Lcvd_p1_end:
	v_mul_f32_e32 v2, 0xbfb8aa3b, v162
	v_mul_f32_e32 v6, 0xbfb8aa3b, v163
	v_exp_f32_e32 v2, v2
	v_exp_f32_e32 v6, v6
	v_mul_f32_e32 v7, 0xbfb8aa3b, v164
	v_mul_f32_e32 v8, 0xbfb8aa3b, v165
	v_add_f32_e32 v2, 1.0, v2
	v_add_f32_e32 v6, 1.0, v6
	v_exp_f32_e32 v7, v7
	v_exp_f32_e32 v8, v8
	v_mul_f32_e32 v9, 0xbfb8aa3b, v154
	v_mul_f32_e32 v10, 0xbfb8aa3b, v155
	v_rcp_f32_e32 v2, v2
	v_rcp_f32_e32 v6, v6
	v_exp_f32_e32 v9, v9
	v_exp_f32_e32 v10, v10
	v_add_f32_e32 v7, 1.0, v7
	v_add_f32_e32 v8, 1.0, v8
	v_mul_f32_e32 v11, 0xbfb8aa3b, v156
	v_mul_f32_e32 v12, 0xbfb8aa3b, v157
	v_mul_f32_e32 v2, v162, v2
	v_mul_f32_e32 v6, v163, v6
	v_rcp_f32_e32 v7, v7
	v_rcp_f32_e32 v8, v8
	v_add_f32_e32 v9, 1.0, v9
	v_add_f32_e32 v10, 1.0, v10
	v_exp_f32_e32 v11, v11
	v_exp_f32_e32 v12, v12
	v_mul_f32_e32 v2, v2, v158
	v_mul_f32_e32 v6, v6, v159
	v_rcp_f32_e32 v9, v9
	v_rcp_f32_e32 v10, v10
	v_med3_f32 v2, v2, s7, v228
	v_med3_f32 v13, v6, s7, v228
	v_mov_b32_e32 v6, v3
	v_cvt_pk_fp8_f32 v6, v2, v13
	v_mul_f32_e32 v7, v164, v7
	v_mul_f32_e32 v8, v165, v8
	v_add_f32_e32 v11, 1.0, v11
	v_add_f32_e32 v12, 1.0, v12
	v_mul_f32_e32 v7, v7, v160
	v_mul_f32_e32 v8, v8, v161
	v_mul_f32_e32 v9, v154, v9
	v_mul_f32_e32 v10, v155, v10
	v_rcp_f32_e32 v11, v11
	v_rcp_f32_e32 v12, v12
	v_mul_f32_e32 v9, v9, v150
	v_mul_f32_e32 v10, v10, v151
	v_med3_f32 v2, v7, s7, v228
	v_med3_f32 v7, v8, s7, v228
	v_cvt_pk_fp8_f32 v6, v2, v7 op_sel:[0,0,1]
	v_med3_f32 v2, v9, s7, v228
	v_med3_f32 v8, v10, s7, v228
	v_mov_b32_e32 v7, v3
	v_cvt_pk_fp8_f32 v7, v2, v8
	v_lshl_add_u32 v4, s48, 8, v181
	v_mul_f32_e32 v11, v156, v11
	v_mul_f32_e32 v12, v157, v12
	v_ashrrev_i32_e32 v5, 31, v4
	v_mul_f32_e32 v11, v11, v152
	v_mul_f32_e32 v12, v12, v153
	v_lshlrev_b64 v[4:5], 11, v[4:5]
	s_lshl_b32 s0, s3, 7
	v_med3_f32 v2, v11, s7, v228
	v_med3_f32 v8, v12, s7, v228
	v_lshl_add_u64 v[4:5], s[40:41], 0, v[4:5]
	s_ashr_i32 s1, s0, 31
	v_cvt_pk_fp8_f32 v7, v2, v8 op_sel:[0,0,1]
	v_lshl_add_u64 v[4:5], v[4:5], 0, s[0:1]
	v_lshl_add_u64 v[4:5], v[4:5], 0, s[76:77]
	v_lshl_add_u64 v[4:5], v[4:5], 0, v[170:171]
	s_nop 15
	s_nop 15
	global_store_dwordx2 v[4:5], v[6:7], off
	v_mul_f32_e32 v2, 0xbfb8aa3b, v146
	v_mul_f32_e32 v6, 0xbfb8aa3b, v147
	v_exp_f32_e32 v2, v2
	v_exp_f32_e32 v6, v6
	v_mul_f32_e32 v7, 0xbfb8aa3b, v148
	v_mul_f32_e32 v8, 0xbfb8aa3b, v149
	v_add_f32_e32 v2, 1.0, v2
	v_add_f32_e32 v6, 1.0, v6
	v_exp_f32_e32 v7, v7
	v_exp_f32_e32 v8, v8
	v_mul_f32_e32 v9, 0xbfb8aa3b, v138
	v_mul_f32_e32 v10, 0xbfb8aa3b, v139
	v_rcp_f32_e32 v2, v2
	v_rcp_f32_e32 v6, v6
	v_exp_f32_e32 v9, v9
	v_exp_f32_e32 v10, v10
	v_add_f32_e32 v7, 1.0, v7
	v_add_f32_e32 v8, 1.0, v8
	v_mul_f32_e32 v11, 0xbfb8aa3b, v140
	v_mul_f32_e32 v12, 0xbfb8aa3b, v141
	v_mul_f32_e32 v2, v146, v2
	v_mul_f32_e32 v6, v147, v6
	v_rcp_f32_e32 v7, v7
	v_rcp_f32_e32 v8, v8
	v_add_f32_e32 v9, 1.0, v9
	v_add_f32_e32 v10, 1.0, v10
	v_exp_f32_e32 v11, v11
	v_exp_f32_e32 v12, v12
	v_mul_f32_e32 v2, v2, v142
	v_mul_f32_e32 v6, v6, v143
	v_rcp_f32_e32 v9, v9
	v_rcp_f32_e32 v10, v10
	v_med3_f32 v2, v2, s7, v228
	v_med3_f32 v13, v6, s7, v228
	v_mov_b32_e32 v6, v3
	v_cvt_pk_fp8_f32 v6, v2, v13
	v_mul_f32_e32 v7, v148, v7
	v_mul_f32_e32 v8, v149, v8
	v_add_f32_e32 v11, 1.0, v11
	v_add_f32_e32 v12, 1.0, v12
	v_mul_f32_e32 v7, v7, v144
	v_mul_f32_e32 v8, v8, v145
	v_mul_f32_e32 v9, v138, v9
	v_mul_f32_e32 v10, v139, v10
	v_rcp_f32_e32 v11, v11
	v_rcp_f32_e32 v12, v12
	v_mul_f32_e32 v9, v9, v134
	v_mul_f32_e32 v10, v10, v135
	v_med3_f32 v2, v7, s7, v228
	v_med3_f32 v7, v8, s7, v228
	v_cvt_pk_fp8_f32 v6, v2, v7 op_sel:[0,0,1]
	v_med3_f32 v2, v9, s7, v228
	v_med3_f32 v8, v10, s7, v228
	v_mov_b32_e32 v7, v3
	v_cvt_pk_fp8_f32 v7, v2, v8
	v_mul_f32_e32 v11, v140, v11
	v_mul_f32_e32 v12, v141, v12
	v_mul_f32_e32 v11, v11, v136
	v_mul_f32_e32 v12, v12, v137
	v_med3_f32 v2, v11, s7, v228
	v_med3_f32 v8, v12, s7, v228
	v_cvt_pk_fp8_f32 v7, v2, v8 op_sel:[0,0,1]
	v_add_co_u32_e32 v8, vcc, s31, v4
	v_mul_f32_e32 v2, 0xbfb8aa3b, v130
	s_nop 0
	v_addc_co_u32_e32 v9, vcc, 0, v5, vcc
	global_store_dwordx2 v[8:9], v[6:7], off
	v_mul_f32_e32 v6, 0xbfb8aa3b, v131
	v_exp_f32_e32 v2, v2
	v_exp_f32_e32 v6, v6
	v_mul_f32_e32 v7, 0xbfb8aa3b, v132
	v_mul_f32_e32 v8, 0xbfb8aa3b, v133
	v_add_f32_e32 v2, 1.0, v2
	v_add_f32_e32 v6, 1.0, v6
	v_exp_f32_e32 v7, v7
	v_exp_f32_e32 v8, v8
	v_mul_f32_e32 v9, 0xbfb8aa3b, v122
	v_mul_f32_e32 v10, 0xbfb8aa3b, v123
	v_rcp_f32_e32 v2, v2
	v_rcp_f32_e32 v6, v6
	v_exp_f32_e32 v9, v9
	v_exp_f32_e32 v10, v10
	v_add_f32_e32 v7, 1.0, v7
	v_add_f32_e32 v8, 1.0, v8
	v_mul_f32_e32 v11, 0xbfb8aa3b, v124
	v_mul_f32_e32 v12, 0xbfb8aa3b, v125
	v_mul_f32_e32 v2, v130, v2
	v_mul_f32_e32 v6, v131, v6
	v_rcp_f32_e32 v7, v7
	v_rcp_f32_e32 v8, v8
	v_add_f32_e32 v9, 1.0, v9
	v_add_f32_e32 v10, 1.0, v10
	v_exp_f32_e32 v11, v11
	v_exp_f32_e32 v12, v12
	v_mul_f32_e32 v2, v2, v126
	v_mul_f32_e32 v6, v6, v127
	v_rcp_f32_e32 v9, v9
	v_rcp_f32_e32 v10, v10
	v_med3_f32 v2, v2, s7, v228
	v_med3_f32 v13, v6, s7, v228
	v_mov_b32_e32 v6, v3
	v_cvt_pk_fp8_f32 v6, v2, v13
	v_mul_f32_e32 v7, v132, v7
	v_mul_f32_e32 v8, v133, v8
	v_add_f32_e32 v11, 1.0, v11
	v_add_f32_e32 v12, 1.0, v12
	v_mul_f32_e32 v7, v7, v128
	v_mul_f32_e32 v8, v8, v129
	v_mul_f32_e32 v9, v122, v9
	v_mul_f32_e32 v10, v123, v10
	v_rcp_f32_e32 v11, v11
	v_rcp_f32_e32 v12, v12
	v_mul_f32_e32 v9, v9, v118
	v_mul_f32_e32 v10, v10, v119
	v_med3_f32 v2, v7, s7, v228
	v_med3_f32 v7, v8, s7, v228
	v_cvt_pk_fp8_f32 v6, v2, v7 op_sel:[0,0,1]
	v_med3_f32 v2, v9, s7, v228
	v_med3_f32 v8, v10, s7, v228
	v_mov_b32_e32 v7, v3
	v_cvt_pk_fp8_f32 v7, v2, v8
	v_mul_f32_e32 v11, v124, v11
	v_mul_f32_e32 v12, v125, v12
	v_mul_f32_e32 v11, v11, v120
	v_mul_f32_e32 v12, v12, v121
	v_med3_f32 v2, v11, s7, v228
	v_med3_f32 v8, v12, s7, v228
	v_cvt_pk_fp8_f32 v7, v2, v8 op_sel:[0,0,1]
	s_mov_b32 s0, 0x10000
	v_add_co_u32_e32 v8, vcc, s0, v4
	v_mul_f32_e32 v2, 0xbfb8aa3b, v112
	s_nop 0
	v_addc_co_u32_e32 v9, vcc, 0, v5, vcc
	global_store_dwordx2 v[8:9], v[6:7], off
	v_mul_f32_e32 v6, 0xbfb8aa3b, v113
	v_exp_f32_e32 v2, v2
	v_exp_f32_e32 v6, v6
	v_mul_f32_e32 v7, 0xbfb8aa3b, v114
	v_mul_f32_e32 v8, 0xbfb8aa3b, v115
	v_add_f32_e32 v2, 1.0, v2
	v_add_f32_e32 v6, 1.0, v6
	v_exp_f32_e32 v7, v7
	v_exp_f32_e32 v8, v8
	v_mul_f32_e32 v9, 0xbfb8aa3b, v104
	v_mul_f32_e32 v10, 0xbfb8aa3b, v105
	v_rcp_f32_e32 v2, v2
	v_rcp_f32_e32 v6, v6
	v_exp_f32_e32 v9, v9
	v_exp_f32_e32 v10, v10
	v_add_f32_e32 v7, 1.0, v7
	v_add_f32_e32 v8, 1.0, v8
	v_mul_f32_e32 v11, 0xbfb8aa3b, v106
	v_mul_f32_e32 v12, 0xbfb8aa3b, v107
	v_mul_f32_e32 v2, v112, v2
	v_mul_f32_e32 v6, v113, v6
	v_rcp_f32_e32 v7, v7
	v_rcp_f32_e32 v8, v8
	v_add_f32_e32 v9, 1.0, v9
	v_add_f32_e32 v10, 1.0, v10
	v_exp_f32_e32 v11, v11
	v_exp_f32_e32 v12, v12
	v_mul_f32_e32 v2, v2, v108
	v_mul_f32_e32 v6, v6, v109
	v_rcp_f32_e32 v9, v9
	v_rcp_f32_e32 v10, v10
	v_med3_f32 v2, v2, s7, v228
	v_med3_f32 v13, v6, s7, v228
	v_mov_b32_e32 v6, v3
	v_cvt_pk_fp8_f32 v6, v2, v13
	v_mul_f32_e32 v7, v114, v7
	v_mul_f32_e32 v8, v115, v8
	v_add_f32_e32 v11, 1.0, v11
	v_add_f32_e32 v12, 1.0, v12
	v_mul_f32_e32 v7, v7, v110
	v_mul_f32_e32 v8, v8, v111
	v_mul_f32_e32 v9, v104, v9
	v_mul_f32_e32 v10, v105, v10
	v_rcp_f32_e32 v11, v11
	v_rcp_f32_e32 v12, v12
	v_mul_f32_e32 v9, v9, v100
	v_mul_f32_e32 v10, v10, v101
	v_med3_f32 v2, v7, s7, v228
	v_med3_f32 v7, v8, s7, v228
	v_cvt_pk_fp8_f32 v6, v2, v7 op_sel:[0,0,1]
	v_med3_f32 v2, v9, s7, v228
	v_med3_f32 v8, v10, s7, v228
	v_mov_b32_e32 v7, v3
	v_cvt_pk_fp8_f32 v7, v2, v8
	v_mul_f32_e32 v11, v106, v11
	v_mul_f32_e32 v12, v107, v12
	v_mul_f32_e32 v11, v11, v102
	v_mul_f32_e32 v12, v12, v103
	v_med3_f32 v2, v11, s7, v228
	v_med3_f32 v8, v12, s7, v228
	v_cvt_pk_fp8_f32 v7, v2, v8 op_sel:[0,0,1]
	s_mov_b32 s0, 0x18000
	v_add_co_u32_e32 v8, vcc, s0, v4
	v_mul_f32_e32 v2, 0xbfb8aa3b, v96
	s_nop 0
	v_addc_co_u32_e32 v9, vcc, 0, v5, vcc
	global_store_dwordx2 v[8:9], v[6:7], off
	v_mul_f32_e32 v6, 0xbfb8aa3b, v97
	v_exp_f32_e32 v2, v2
	v_exp_f32_e32 v6, v6
	v_mul_f32_e32 v7, 0xbfb8aa3b, v98
	v_mul_f32_e32 v8, 0xbfb8aa3b, v99
	v_add_f32_e32 v2, 1.0, v2
	v_add_f32_e32 v6, 1.0, v6
	v_exp_f32_e32 v7, v7
	v_exp_f32_e32 v8, v8
	v_mul_f32_e32 v9, 0xbfb8aa3b, v88
	v_mul_f32_e32 v10, 0xbfb8aa3b, v89
	v_rcp_f32_e32 v2, v2
	v_rcp_f32_e32 v6, v6
	v_exp_f32_e32 v9, v9
	v_exp_f32_e32 v10, v10
	v_add_f32_e32 v7, 1.0, v7
	v_add_f32_e32 v8, 1.0, v8
	v_mul_f32_e32 v11, 0xbfb8aa3b, v90
	v_mul_f32_e32 v12, 0xbfb8aa3b, v91
	v_mul_f32_e32 v2, v96, v2
	v_mul_f32_e32 v6, v97, v6
	v_rcp_f32_e32 v7, v7
	v_rcp_f32_e32 v8, v8
	v_add_f32_e32 v9, 1.0, v9
	v_add_f32_e32 v10, 1.0, v10
	v_exp_f32_e32 v11, v11
	v_exp_f32_e32 v12, v12
	v_mul_f32_e32 v2, v2, v92
	v_mul_f32_e32 v6, v6, v93
	v_rcp_f32_e32 v9, v9
	v_rcp_f32_e32 v10, v10
	v_med3_f32 v2, v2, s7, v228
	v_med3_f32 v13, v6, s7, v228
	v_mov_b32_e32 v6, v3
	v_cvt_pk_fp8_f32 v6, v2, v13
	v_mul_f32_e32 v7, v98, v7
	v_mul_f32_e32 v8, v99, v8
	v_add_f32_e32 v11, 1.0, v11
	v_add_f32_e32 v12, 1.0, v12
	v_mul_f32_e32 v7, v7, v94
	v_mul_f32_e32 v8, v8, v95
	v_mul_f32_e32 v9, v88, v9
	v_mul_f32_e32 v10, v89, v10
	v_rcp_f32_e32 v11, v11
	v_rcp_f32_e32 v12, v12
	v_mul_f32_e32 v9, v9, v84
	v_mul_f32_e32 v10, v10, v85
	v_med3_f32 v2, v7, s7, v228
	v_med3_f32 v7, v8, s7, v228
	v_cvt_pk_fp8_f32 v6, v2, v7 op_sel:[0,0,1]
	v_med3_f32 v2, v9, s7, v228
	v_med3_f32 v8, v10, s7, v228
	v_mov_b32_e32 v7, v3
	v_cvt_pk_fp8_f32 v7, v2, v8
	v_mul_f32_e32 v11, v90, v11
	v_mul_f32_e32 v12, v91, v12
	v_mul_f32_e32 v11, v11, v86
	v_mul_f32_e32 v12, v12, v87
	v_med3_f32 v2, v11, s7, v228
	v_med3_f32 v8, v12, s7, v228
	v_cvt_pk_fp8_f32 v7, v2, v8 op_sel:[0,0,1]
	v_add_co_u32_e32 v8, vcc, s16, v4
	v_mul_f32_e32 v2, 0xbfb8aa3b, v80
	s_nop 0
	v_addc_co_u32_e32 v9, vcc, 0, v5, vcc
	global_store_dwordx2 v[8:9], v[6:7], off
	v_mul_f32_e32 v6, 0xbfb8aa3b, v81
	v_exp_f32_e32 v2, v2
	v_exp_f32_e32 v6, v6
	v_mul_f32_e32 v7, 0xbfb8aa3b, v82
	v_mul_f32_e32 v8, 0xbfb8aa3b, v83
	v_add_f32_e32 v2, 1.0, v2
	v_add_f32_e32 v6, 1.0, v6
	v_exp_f32_e32 v7, v7
	v_exp_f32_e32 v8, v8
	v_mul_f32_e32 v9, 0xbfb8aa3b, v72
	v_mul_f32_e32 v10, 0xbfb8aa3b, v73
	v_rcp_f32_e32 v2, v2
	v_rcp_f32_e32 v6, v6
	v_exp_f32_e32 v9, v9
	v_exp_f32_e32 v10, v10
	v_add_f32_e32 v7, 1.0, v7
	v_add_f32_e32 v8, 1.0, v8
	v_mul_f32_e32 v11, 0xbfb8aa3b, v74
	v_mul_f32_e32 v12, 0xbfb8aa3b, v75
	v_mul_f32_e32 v2, v80, v2
	v_mul_f32_e32 v6, v81, v6
	v_rcp_f32_e32 v7, v7
	v_rcp_f32_e32 v8, v8
	v_add_f32_e32 v9, 1.0, v9
	v_add_f32_e32 v10, 1.0, v10
	v_exp_f32_e32 v11, v11
	v_exp_f32_e32 v12, v12
	v_mul_f32_e32 v2, v2, v76
	v_mul_f32_e32 v6, v6, v77
	v_rcp_f32_e32 v9, v9
	v_rcp_f32_e32 v10, v10
	v_med3_f32 v2, v2, s7, v228
	v_med3_f32 v13, v6, s7, v228
	v_mov_b32_e32 v6, v3
	v_cvt_pk_fp8_f32 v6, v2, v13
	v_mul_f32_e32 v7, v82, v7
	v_mul_f32_e32 v8, v83, v8
	v_add_f32_e32 v11, 1.0, v11
	v_add_f32_e32 v12, 1.0, v12
	v_mul_f32_e32 v7, v7, v78
	v_mul_f32_e32 v8, v8, v79
	v_mul_f32_e32 v9, v72, v9
	v_mul_f32_e32 v10, v73, v10
	v_rcp_f32_e32 v11, v11
	v_rcp_f32_e32 v12, v12
	v_mul_f32_e32 v9, v9, v68
	v_mul_f32_e32 v10, v10, v69
	v_med3_f32 v2, v7, s7, v228
	v_med3_f32 v7, v8, s7, v228
	v_cvt_pk_fp8_f32 v6, v2, v7 op_sel:[0,0,1]
	v_med3_f32 v2, v9, s7, v228
	v_med3_f32 v8, v10, s7, v228
	v_mov_b32_e32 v7, v3
	v_cvt_pk_fp8_f32 v7, v2, v8
	v_mul_f32_e32 v11, v74, v11
	v_mul_f32_e32 v12, v75, v12
	v_mul_f32_e32 v11, v11, v70
	v_mul_f32_e32 v12, v12, v71
	v_med3_f32 v2, v11, s7, v228
	v_med3_f32 v8, v12, s7, v228
	v_cvt_pk_fp8_f32 v7, v2, v8 op_sel:[0,0,1]
	s_mov_b32 s0, 0x48000
	v_add_co_u32_e32 v8, vcc, s0, v4
	v_mul_f32_e32 v2, 0xbfb8aa3b, v60
	s_nop 0
	v_addc_co_u32_e32 v9, vcc, 0, v5, vcc
	global_store_dwordx2 v[8:9], v[6:7], off
	v_mul_f32_e32 v6, 0xbfb8aa3b, v61
	v_exp_f32_e32 v2, v2
	v_exp_f32_e32 v6, v6
	v_mul_f32_e32 v7, 0xbfb8aa3b, v62
	v_mul_f32_e32 v8, 0xbfb8aa3b, v63
	v_add_f32_e32 v2, 1.0, v2
	v_add_f32_e32 v6, 1.0, v6
	v_exp_f32_e32 v7, v7
	v_exp_f32_e32 v8, v8
	v_mul_f32_e32 v9, 0xbfb8aa3b, v52
	v_mul_f32_e32 v10, 0xbfb8aa3b, v53
	v_rcp_f32_e32 v2, v2
	v_rcp_f32_e32 v6, v6
	v_exp_f32_e32 v9, v9
	v_exp_f32_e32 v10, v10
	v_add_f32_e32 v7, 1.0, v7
	v_add_f32_e32 v8, 1.0, v8
	v_mul_f32_e32 v11, 0xbfb8aa3b, v54
	v_mul_f32_e32 v12, 0xbfb8aa3b, v55
	v_mul_f32_e32 v2, v60, v2
	v_mul_f32_e32 v6, v61, v6
	v_rcp_f32_e32 v7, v7
	v_rcp_f32_e32 v8, v8
	v_add_f32_e32 v9, 1.0, v9
	v_add_f32_e32 v10, 1.0, v10
	v_exp_f32_e32 v11, v11
	v_exp_f32_e32 v12, v12
	v_mul_f32_e32 v2, v2, v64
	v_mul_f32_e32 v6, v6, v65
	v_rcp_f32_e32 v9, v9
	v_rcp_f32_e32 v10, v10
	v_med3_f32 v2, v2, s7, v228
	v_med3_f32 v13, v6, s7, v228
	v_mov_b32_e32 v6, v3
	v_cvt_pk_fp8_f32 v6, v2, v13
	v_mul_f32_e32 v7, v62, v7
	v_mul_f32_e32 v8, v63, v8
	v_add_f32_e32 v11, 1.0, v11
	v_add_f32_e32 v12, 1.0, v12
	v_mul_f32_e32 v7, v7, v66
	v_mul_f32_e32 v8, v8, v67
	v_mul_f32_e32 v9, v52, v9
	v_mul_f32_e32 v10, v53, v10
	v_rcp_f32_e32 v11, v11
	v_rcp_f32_e32 v12, v12
	v_mul_f32_e32 v9, v9, v56
	v_mul_f32_e32 v10, v10, v57
	v_med3_f32 v2, v7, s7, v228
	v_med3_f32 v7, v8, s7, v228
	v_cvt_pk_fp8_f32 v6, v2, v7 op_sel:[0,0,1]
	v_med3_f32 v2, v9, s7, v228
	v_med3_f32 v8, v10, s7, v228
	v_mov_b32_e32 v7, v3
	v_cvt_pk_fp8_f32 v7, v2, v8
	v_mul_f32_e32 v11, v54, v11
	v_mul_f32_e32 v12, v55, v12
	v_mul_f32_e32 v11, v11, v58
	v_mul_f32_e32 v12, v12, v59
	v_med3_f32 v2, v11, s7, v228
	v_med3_f32 v8, v12, s7, v228
	v_cvt_pk_fp8_f32 v7, v2, v8 op_sel:[0,0,1]
	s_mov_b32 s0, 0x50000
	v_add_co_u32_e32 v8, vcc, s0, v4
	v_mul_f32_e32 v2, 0xbfb8aa3b, v44
	s_nop 0
	v_addc_co_u32_e32 v9, vcc, 0, v5, vcc
	global_store_dwordx2 v[8:9], v[6:7], off
	v_mul_f32_e32 v6, 0xbfb8aa3b, v45
	v_exp_f32_e32 v2, v2
	v_exp_f32_e32 v6, v6
	v_mul_f32_e32 v7, 0xbfb8aa3b, v46
	v_mul_f32_e32 v8, 0xbfb8aa3b, v47
	v_add_f32_e32 v2, 1.0, v2
	v_add_f32_e32 v6, 1.0, v6
	v_exp_f32_e32 v7, v7
	v_exp_f32_e32 v8, v8
	v_mul_f32_e32 v9, 0xbfb8aa3b, v36
	v_mul_f32_e32 v10, 0xbfb8aa3b, v37
	v_rcp_f32_e32 v2, v2
	v_rcp_f32_e32 v6, v6
	v_exp_f32_e32 v9, v9
	v_exp_f32_e32 v10, v10
	v_add_f32_e32 v7, 1.0, v7
	v_add_f32_e32 v8, 1.0, v8
	v_mul_f32_e32 v11, 0xbfb8aa3b, v38
	v_mul_f32_e32 v12, 0xbfb8aa3b, v39
	v_mul_f32_e32 v2, v44, v2
	v_mul_f32_e32 v6, v45, v6
	v_rcp_f32_e32 v7, v7
	v_rcp_f32_e32 v8, v8
	v_add_f32_e32 v9, 1.0, v9
	v_add_f32_e32 v10, 1.0, v10
	v_exp_f32_e32 v11, v11
	v_exp_f32_e32 v12, v12
	v_mul_f32_e32 v2, v2, v48
	v_mul_f32_e32 v6, v6, v49
	v_rcp_f32_e32 v9, v9
	v_rcp_f32_e32 v10, v10
	v_med3_f32 v2, v2, s7, v228
	v_med3_f32 v13, v6, s7, v228
	v_mov_b32_e32 v6, v3
	v_cvt_pk_fp8_f32 v6, v2, v13
	v_mul_f32_e32 v7, v46, v7
	v_mul_f32_e32 v8, v47, v8
	v_add_f32_e32 v11, 1.0, v11
	v_add_f32_e32 v12, 1.0, v12
	v_mul_f32_e32 v7, v7, v50
	v_mul_f32_e32 v8, v8, v51
	v_mul_f32_e32 v9, v36, v9
	v_mul_f32_e32 v10, v37, v10
	v_rcp_f32_e32 v11, v11
	v_rcp_f32_e32 v12, v12
	v_mul_f32_e32 v9, v9, v40
	v_mul_f32_e32 v10, v10, v41
	v_med3_f32 v2, v7, s7, v228
	v_med3_f32 v7, v8, s7, v228
	v_cvt_pk_fp8_f32 v6, v2, v7 op_sel:[0,0,1]
	v_med3_f32 v2, v9, s7, v228
	v_med3_f32 v8, v10, s7, v228
	v_mov_b32_e32 v7, v3
	v_cvt_pk_fp8_f32 v7, v2, v8
	v_mul_f32_e32 v11, v38, v11
	v_mul_f32_e32 v12, v39, v12
	v_mul_f32_e32 v11, v11, v42
	v_mul_f32_e32 v12, v12, v43
	v_med3_f32 v2, v11, s7, v228
	v_med3_f32 v8, v12, s7, v228
	v_cvt_pk_fp8_f32 v7, v2, v8 op_sel:[0,0,1]
	v_add_co_u32_e32 v4, vcc, 0x58000, v4
	v_mov_b32_e32 v176, v204
	s_nop 0
	v_addc_co_u32_e32 v5, vcc, 0, v5, vcc
	s_and_b64 vcc, exec, s[38:39]
	v_mov_b32_e32 v178, v205
	v_mov_b32_e32 v180, v203
	v_mov_b32_e32 v184, v202
	s_mov_b32 s3, s44
	s_mov_b32 s48, s42
	s_mov_b64 s[50:51], s[46:47]
	global_store_dwordx2 v[4:5], v[6:7], off
	s_lshr_b32 s72, s2, 3
	s_xor_b32 s72, s72, s32
	s_and_b32 s72, s72, 1
	s_cbranch_scc1 .Lcvd_p2_end
	s_cmpk_ge_u32 s32, 14
	s_cbranch_scc1 .Lcvd_p2_end
	v_readlane_b32 s72, v255, 44
	s_lshr_b32 s80, s32, 1
	s_lshl_b32 s80, s80, 10
	s_add_i32 s80, s80, s2
	s_nop 0
	s_add_i32 s72, s72, s80
	s_cmpk_ge_i32 s72, 7136
	s_cbranch_scc1 .Lcvd_p2_end
	s_addk_i32 s72, 1056
	v_readlane_b32 s78, v255, 42
	v_readlane_b32 s79, v255, 43
	s_lshr_b32 s80, s72, 9
	s_lshl_b32 s80, s80, 21
	s_and_b32 s81, s72, 15
	s_lshl_b32 s81, s81, 17
	s_add_i32 s80, s80, s81
	s_bfe_u32 s81, s72, 0x50004
	s_lshl_b32 s81, s81, 6
	s_add_i32 s80, s80, s81
	v_and_b32_e32 v22, 15, v0
	v_lshlrev_b32_e32 v22, 13, v22
	v_bfe_u32 v23, v0, 4, 2
	v_lshl_add_u32 v22, v23, 3, v22
	v_add_u32_e32 v22, s80, v22
	v_add_u32_e32 v23, 0x1000, v22
	s_waitcnt vmcnt(8)
	v_mul_f32_e32 v210, 0x42800000, v210
	v_mul_f32_e32 v211, 0x42800000, v211
	v_mul_f32_e32 v212, 0x42800000, v212
	v_mul_f32_e32 v213, 0x42800000, v213
	v_mul_f32_e32 v214, 0x42800000, v214
	v_mul_f32_e32 v215, 0x42800000, v215
	v_mul_f32_e32 v216, 0x42800000, v216
	v_mul_f32_e32 v217, 0x42800000, v217
	v_mul_f32_e32 v218, 0x42800000, v218
	v_mul_f32_e32 v219, 0x42800000, v219
	v_mul_f32_e32 v220, 0x42800000, v220
	v_mul_f32_e32 v221, 0x42800000, v221
	v_mul_f32_e32 v222, 0x42800000, v222
	v_mul_f32_e32 v223, 0x42800000, v223
	v_mul_f32_e32 v224, 0x42800000, v224
	v_mul_f32_e32 v225, 0x42800000, v225
	v_mul_f32_e32 v230, 0x42800000, v230
	v_mul_f32_e32 v231, 0x42800000, v231
	v_mul_f32_e32 v232, 0x42800000, v232
	v_mul_f32_e32 v233, 0x42800000, v233
	v_mul_f32_e32 v234, 0x42800000, v234
	v_mul_f32_e32 v235, 0x42800000, v235
	v_mul_f32_e32 v236, 0x42800000, v236
	v_mul_f32_e32 v237, 0x42800000, v237
	v_mul_f32_e32 v240, 0x42800000, v240
	v_mul_f32_e32 v241, 0x42800000, v241
	v_mul_f32_e32 v242, 0x42800000, v242
	v_mul_f32_e32 v243, 0x42800000, v243
	v_mul_f32_e32 v244, 0x42800000, v244
	v_mul_f32_e32 v245, 0x42800000, v245
	v_mul_f32_e32 v246, 0x42800000, v246
	v_mul_f32_e32 v247, 0x42800000, v247
	v_med3_f32 v210, v210, s7, v228
	v_med3_f32 v211, v211, s7, v228
	v_med3_f32 v212, v212, s7, v228
	v_med3_f32 v213, v213, s7, v228
	v_med3_f32 v214, v214, s7, v228
	v_med3_f32 v215, v215, s7, v228
	v_med3_f32 v216, v216, s7, v228
	v_med3_f32 v217, v217, s7, v228
	v_med3_f32 v218, v218, s7, v228
	v_med3_f32 v219, v219, s7, v228
	v_med3_f32 v220, v220, s7, v228
	v_med3_f32 v221, v221, s7, v228
	v_med3_f32 v222, v222, s7, v228
	v_med3_f32 v223, v223, s7, v228
	v_med3_f32 v224, v224, s7, v228
	v_med3_f32 v225, v225, s7, v228
	v_med3_f32 v230, v230, s7, v228
	v_med3_f32 v231, v231, s7, v228
	v_med3_f32 v232, v232, s7, v228
	v_med3_f32 v233, v233, s7, v228
	v_med3_f32 v234, v234, s7, v228
	v_med3_f32 v235, v235, s7, v228
	v_med3_f32 v236, v236, s7, v228
	v_med3_f32 v237, v237, s7, v228
	v_med3_f32 v240, v240, s7, v228
	v_med3_f32 v241, v241, s7, v228
	v_med3_f32 v242, v242, s7, v228
	v_med3_f32 v243, v243, s7, v228
	v_med3_f32 v244, v244, s7, v228
	v_med3_f32 v245, v245, s7, v228
	v_med3_f32 v246, v246, s7, v228
	v_med3_f32 v247, v247, s7, v228
	v_cvt_pk_fp8_f32 v14, v210, v214
	v_cvt_pk_fp8_f32 v15, v230, v234
	v_cvt_pk_fp8_f32 v16, v211, v215
	v_cvt_pk_fp8_f32 v17, v231, v235
	v_cvt_pk_fp8_f32 v18, v212, v216
	v_cvt_pk_fp8_f32 v19, v232, v236
	v_cvt_pk_fp8_f32 v20, v213, v217
	v_cvt_pk_fp8_f32 v21, v233, v237
	v_cvt_pk_fp8_f32 v14, v218, v222 op_sel:[0,0,1]
	v_cvt_pk_fp8_f32 v15, v240, v244 op_sel:[0,0,1]
	v_cvt_pk_fp8_f32 v16, v219, v223 op_sel:[0,0,1]
	v_cvt_pk_fp8_f32 v17, v241, v245 op_sel:[0,0,1]
	v_cvt_pk_fp8_f32 v18, v220, v224 op_sel:[0,0,1]
	v_cvt_pk_fp8_f32 v19, v242, v246 op_sel:[0,0,1]
	v_cvt_pk_fp8_f32 v20, v221, v225 op_sel:[0,0,1]
	v_cvt_pk_fp8_f32 v21, v243, v247 op_sel:[0,0,1]
	s_nop 1
	global_store_dwordx2 v22, v[14:15], s[78:79]
	global_store_dwordx2 v22, v[16:17], s[78:79] offset:2048
	global_store_dwordx2 v23, v[18:19], s[78:79]
	global_store_dwordx2 v23, v[20:21], s[78:79] offset:2048
